# v041 + tile-loop head drains (QKV, in-proj u/vT, GEMM2) turned into counted waits that leave the previous tile's result stores in flight
# speedup vs baseline: 1.0018x; 1.0018x over previous
.LBB0_116:
	s_lshl_b32 s30, s7, 6
	s_add_u32 s31, s0, 0x3fe00000
	s_addc_u32 s34, s1, 0
	s_add_u32 s0, s68, 0x80
	s_addc_u32 s1, s69, 0
	s_add_i32 s35, s15, 0x18000
	v_mov_b32_e32 v4, v230
	s_waitcnt vmcnt(4)
	s_barrier
	s_mov_b32 m0, s35
	s_mul_i32 s10, s28, 0xc0
	global_load_lds_dwordx4 v4, s[0:1]
	s_add_u32 s0, s68, 0x20080
	s_addc_u32 s1, s69, 0
	v_mov_b32_e32 v4, v230
	s_add_i32 s36, s15, 0x1a000
	s_mov_b32 m0, s36
	v_readlane_b32 s58, v255, 30
	global_load_lds_dwordx4 v4, s[0:1]
	s_add_u32 s0, s46, 0x80
	s_addc_u32 s1, s47, 0
	v_mov_b32_e32 v4, v229
	s_add_i32 s37, s15, 0x8000
	s_mov_b32 m0, s37
	v_add_u32_e32 v231, 0, v2
	global_load_lds_dwordx4 v4, s[0:1]
	s_add_u32 s0, s46, 0x10080
	s_addc_u32 s1, s47, 0
	v_mov_b32_e32 v4, v229
	s_add_i32 s70, s15, 0xa000
	s_mov_b32 m0, s70
	s_add_i32 s71, s15, 0x1c000
	global_load_lds_dwordx4 v4, s[0:1]
	s_add_u32 s0, s68, 0x8080
	s_addc_u32 s1, s69, 0
	v_mov_b32_e32 v4, v230
	s_mov_b32 m0, s71
	v_add_u32_e32 v232, 0, v3
	global_load_lds_dwordx4 v4, s[0:1]
	s_add_u32 s0, s68, 0x28080
	s_addc_u32 s1, s69, 0
	s_add_i32 s72, s15, 0x1e000
	v_mov_b32_e32 v4, v230
	s_mov_b32 m0, s72
	s_cmpk_lt_u32 s6, 0x100
	global_load_lds_dwordx4 v4, s[0:1]
	s_waitcnt vmcnt(0)
	v_readlane_b32 s0, v255, 14
	s_cselect_b64 s[54:55], -1, 0
	s_mov_b32 s77, s11
	s_lshl_b64 s[56:57], s[10:11], 2
	v_readlane_b32 s59, v255, 31
	v_readlane_b32 s73, v254, 55
	s_mov_b32 s10, s0
	s_movk_i32 s11, 0x121
	v_mov_b32_e32 v225, 0x388637bd
	v_mov_b32_e32 v228, 0x3e800000
	s_barrier
	v_readlane_b32 s1, v255, 15
	s_branch .LBB0_119

.LBB0_121:
	s_ashr_i32 s63, s62, 31
	s_lshl_b64 s[0:1], s[62:63], 18
	s_add_u32 s64, s9, s0
	s_addc_u32 s65, s12, s1
	s_and_b64 s[0:1], s[40:41], exec
	s_cselect_b32 s45, s65, s47
	s_cselect_b32 s44, s64, s46
	s_ashr_i32 s61, s60, 31
	s_lshl_b64 s[0:1], s[60:61], 18
	s_add_u32 s66, s13, s0
	s_addc_u32 s67, s14, s1
	ds_read_b128 v[90:93], v232
	ds_read_b128 v[94:97], v232 offset:1024
	ds_read_b128 v[98:101], v232 offset:2048
	ds_read_b128 v[102:105], v232 offset:3072
	s_and_b64 s[0:1], s[40:41], exec
	s_cselect_b32 s43, s67, s69
	s_cselect_b32 s42, s66, s68
	s_add_u32 s4, s46, 0x100
	s_addc_u32 s5, s47, 0
	s_add_u32 s6, s68, 0x100
	s_addc_u32 s7, s69, 0
	s_add_u32 s0, s46, 0x180
	s_addc_u32 s1, s47, 0
	s_add_u32 s74, s46, 0x20080
	s_addc_u32 s75, s47, 0
	v_mov_b32_e32 v2, v229
	s_add_i32 s61, s15, 0xc000
	ds_read_b128 v[38:41], v231
	ds_read_b128 v[42:45], v231 offset:1024
	ds_read_b128 v[46:49], v231 offset:2048
	ds_read_b128 v[50:53], v231 offset:3072
	ds_read_b128 v[54:57], v231 offset:4096
	ds_read_b128 v[58:61], v231 offset:5120
	ds_read_b128 v[62:65], v231 offset:6144
	s_waitcnt vmcnt(2)
	ds_read_b128 v[66:69], v231 offset:7168
	s_mov_b32 m0, s61
	s_nop 0
	global_load_lds_dwordx4 v2, s[74:75]
	s_add_u32 s74, s46, 0x30080
	s_addc_u32 s75, s47, 0
	s_add_i32 s23, s15, 0xe000
	v_mov_b32_e32 v2, v229
	s_mov_b32 m0, s23
	s_nop 0
	global_load_lds_dwordx4 v2, s[74:75]
	s_waitcnt lgkmcnt(8)
	s_barrier
	s_waitcnt lgkmcnt(0)
	s_setprio 1
	s_waitcnt lgkmcnt(0)
	v_mfma_f32_16x16x128_f8f6f4 v[2:5], v[90:97], v[38:45], 0
	v_mfma_f32_16x16x128_f8f6f4 v[6:9], v[98:105], v[38:45], 0
	v_mfma_f32_16x16x128_f8f6f4 v[10:13], v[90:97], v[46:53], 0
	v_mfma_f32_16x16x128_f8f6f4 v[14:17], v[98:105], v[46:53], 0
	v_mfma_f32_16x16x128_f8f6f4 v[18:21], v[90:97], v[54:61], 0
	v_mfma_f32_16x16x128_f8f6f4 v[22:25], v[98:105], v[54:61], 0
	v_mfma_f32_16x16x128_f8f6f4 v[26:29], v[90:97], v[62:69], 0
	v_mfma_f32_16x16x128_f8f6f4 v[30:33], v[98:105], v[62:69], 0
	s_setprio 0
	s_barrier
	v_mov_b32_e32 v34, v230
	s_mov_b32 m0, s16
	ds_read_b128 v[122:125], v232 offset:16384
	ds_read_b128 v[126:129], v232 offset:17408
	ds_read_b128 v[130:133], v232 offset:18432
	ds_read_b128 v[134:137], v232 offset:19456
	s_nop 0
	global_load_lds_dwordx4 v34, s[6:7]
	s_add_u32 s6, s68, 0x20100
	s_addc_u32 s7, s69, 0
	v_mov_b32_e32 v34, v230
	s_mov_b32 m0, s17
	s_nop 0
	global_load_lds_dwordx4 v34, s[6:7]
	s_barrier
	s_waitcnt lgkmcnt(0)
	s_setprio 1
	s_waitcnt lgkmcnt(0)
	v_mfma_f32_16x16x128_f8f6f4 v[34:37], v[122:129], v[38:45], 0
	v_mfma_f32_16x16x128_f8f6f4 v[38:41], v[130:137], v[38:45], 0
	v_mfma_f32_16x16x128_f8f6f4 v[42:45], v[122:129], v[46:53], 0
	v_mfma_f32_16x16x128_f8f6f4 v[46:49], v[130:137], v[46:53], 0
	v_mfma_f32_16x16x128_f8f6f4 v[50:53], v[122:129], v[54:61], 0
	v_mfma_f32_16x16x128_f8f6f4 v[54:57], v[130:137], v[54:61], 0
	v_mfma_f32_16x16x128_f8f6f4 v[58:61], v[122:129], v[62:69], 0
	v_mfma_f32_16x16x128_f8f6f4 v[62:65], v[130:137], v[62:69], 0
	s_setprio 0
	v_mov_b32_e32 v66, v229
	s_mov_b32 m0, s15
	s_barrier
	ds_read_b128 v[106:109], v231 offset:16384
	ds_read_b128 v[110:113], v231 offset:17408
	ds_read_b128 v[114:117], v231 offset:18432
	ds_read_b128 v[118:121], v231 offset:19456
	ds_read_b128 v[138:141], v231 offset:20480
	ds_read_b128 v[142:145], v231 offset:21504
	ds_read_b128 v[146:149], v231 offset:22528
	ds_read_b128 v[150:153], v231 offset:23552
	s_nop 0
	global_load_lds_dwordx4 v66, s[4:5]
	s_add_u32 s4, s46, 0x10100
	s_addc_u32 s5, s47, 0
	v_mov_b32_e32 v66, v229
	s_mov_b32 m0, s24
	s_nop 0
	global_load_lds_dwordx4 v66, s[4:5]
	s_barrier
	s_waitcnt lgkmcnt(0)
	s_setprio 1
	s_waitcnt lgkmcnt(0)
	v_mfma_f32_16x16x128_f8f6f4 v[66:69], v[90:97], v[106:113], 0
	v_mfma_f32_16x16x128_f8f6f4 v[70:73], v[98:105], v[106:113], 0
	v_mfma_f32_16x16x128_f8f6f4 v[74:77], v[90:97], v[114:121], 0
	v_mfma_f32_16x16x128_f8f6f4 v[78:81], v[98:105], v[114:121], 0
	v_mfma_f32_16x16x128_f8f6f4 v[82:85], v[90:97], v[138:145], 0
	v_mfma_f32_16x16x128_f8f6f4 v[86:89], v[98:105], v[138:145], 0
	v_mfma_f32_16x16x128_f8f6f4 v[90:93], v[90:97], v[146:153], 0
	v_mfma_f32_16x16x128_f8f6f4 v[94:97], v[98:105], v[146:153], 0
	s_setprio 0
	s_barrier
	s_add_u32 s4, s68, 0x8100
	s_addc_u32 s5, s69, 0
	v_mov_b32_e32 v98, v230
	s_mov_b32 m0, s25
	s_nop 0
	global_load_lds_dwordx4 v98, s[4:5]
	s_add_u32 s4, s68, 0x28100
	s_addc_u32 s5, s69, 0
	v_mov_b32_e32 v98, v230
	s_mov_b32 m0, s26
	s_nop 0
	global_load_lds_dwordx4 v98, s[4:5]
	s_waitcnt vmcnt(6)
	s_barrier
	s_setprio 1
	v_mfma_f32_16x16x128_f8f6f4 v[98:101], v[122:129], v[106:113], 0
	v_mfma_f32_16x16x128_f8f6f4 v[102:105], v[130:137], v[106:113], 0
	v_mfma_f32_16x16x128_f8f6f4 v[106:109], v[122:129], v[114:121], 0
	v_mfma_f32_16x16x128_f8f6f4 v[110:113], v[130:137], v[114:121], 0
	v_mfma_f32_16x16x128_f8f6f4 v[114:117], v[122:129], v[138:145], 0
	v_mfma_f32_16x16x128_f8f6f4 v[118:121], v[130:137], v[138:145], 0
	v_mfma_f32_16x16x128_f8f6f4 v[122:125], v[122:129], v[146:153], 0
	v_mfma_f32_16x16x128_f8f6f4 v[126:129], v[130:137], v[146:153], 0
	s_setprio 0
	s_barrier
	ds_read_b128 v[130:133], v232 offset:32768
	ds_read_b128 v[134:137], v232 offset:33792
	ds_read_b128 v[138:141], v232 offset:34816
	ds_read_b128 v[142:145], v232 offset:35840
	s_add_u32 s4, s46, 0x20100
	s_addc_u32 s5, s47, 0
	v_mov_b32_e32 v178, v229
	s_mov_b32 m0, s27
	ds_read_b128 v[146:149], v231 offset:32768
	ds_read_b128 v[150:153], v231 offset:33792
	ds_read_b128 v[154:157], v231 offset:34816
	ds_read_b128 v[158:161], v231 offset:35840
	ds_read_b128 v[162:165], v231 offset:36864
	ds_read_b128 v[166:169], v231 offset:37888
	ds_read_b128 v[170:173], v231 offset:38912
	ds_read_b128 v[174:177], v231 offset:39936
	s_nop 0
	global_load_lds_dwordx4 v178, s[4:5]
	s_add_u32 s4, s46, 0x30100
	s_addc_u32 s5, s47, 0
	v_mov_b32_e32 v178, v229
	s_mov_b32 m0, s29
	s_nop 0
	global_load_lds_dwordx4 v178, s[4:5]
	s_waitcnt lgkmcnt(8)
	s_barrier
	s_waitcnt lgkmcnt(0)
	s_setprio 1
	s_waitcnt lgkmcnt(0)
	v_mfma_f32_16x16x128_f8f6f4 v[2:5], v[130:137], v[146:153], v[2:5]
	v_mfma_f32_16x16x128_f8f6f4 v[6:9], v[138:145], v[146:153], v[6:9]
	v_mfma_f32_16x16x128_f8f6f4 v[10:13], v[130:137], v[154:161], v[10:13]
	v_mfma_f32_16x16x128_f8f6f4 v[14:17], v[138:145], v[154:161], v[14:17]
	v_mfma_f32_16x16x128_f8f6f4 v[18:21], v[130:137], v[162:169], v[18:21]
	v_mfma_f32_16x16x128_f8f6f4 v[22:25], v[138:145], v[162:169], v[22:25]
	v_mfma_f32_16x16x128_f8f6f4 v[26:29], v[130:137], v[170:177], v[26:29]
	v_mfma_f32_16x16x128_f8f6f4 v[30:33], v[138:145], v[170:177], v[30:33]
	s_setprio 0
	s_barrier
	s_add_u32 s4, s68, 0x180
	s_addc_u32 s5, s69, 0
	v_mov_b32_e32 v194, v230
	s_mov_b32 m0, s35
	ds_read_b128 v[178:181], v232 offset:49152
	ds_read_b128 v[182:185], v232 offset:50176
	ds_read_b128 v[186:189], v232 offset:51200
	ds_read_b128 v[190:193], v232 offset:52224
	s_nop 0
	global_load_lds_dwordx4 v194, s[4:5]
	s_add_u32 s4, s68, 0x20180
	s_addc_u32 s5, s69, 0
	v_mov_b32_e32 v194, v230
	s_mov_b32 m0, s36
	s_nop 0
	global_load_lds_dwordx4 v194, s[4:5]
	s_barrier
	s_waitcnt lgkmcnt(0)
	s_setprio 1
	s_waitcnt lgkmcnt(0)
	v_mfma_f32_16x16x128_f8f6f4 v[34:37], v[178:185], v[146:153], v[34:37]
	v_mfma_f32_16x16x128_f8f6f4 v[38:41], v[186:193], v[146:153], v[38:41]
	v_mfma_f32_16x16x128_f8f6f4 v[42:45], v[178:185], v[154:161], v[42:45]
	v_mfma_f32_16x16x128_f8f6f4 v[46:49], v[186:193], v[154:161], v[46:49]
	v_mfma_f32_16x16x128_f8f6f4 v[50:53], v[178:185], v[162:169], v[50:53]
	v_mfma_f32_16x16x128_f8f6f4 v[54:57], v[186:193], v[162:169], v[54:57]
	v_mfma_f32_16x16x128_f8f6f4 v[58:61], v[178:185], v[170:177], v[58:61]
	v_mfma_f32_16x16x128_f8f6f4 v[62:65], v[186:193], v[170:177], v[62:65]
	s_setprio 0
	v_mov_b32_e32 v194, v229
	s_mov_b32 m0, s37
	s_barrier
	ds_read_b128 v[146:149], v231 offset:49152
	ds_read_b128 v[150:153], v231 offset:50176
	ds_read_b128 v[154:157], v231 offset:51200
	ds_read_b128 v[158:161], v231 offset:52224
	ds_read_b128 v[162:165], v231 offset:53248
	ds_read_b128 v[166:169], v231 offset:54272
	ds_read_b128 v[170:173], v231 offset:55296
	ds_read_b128 v[174:177], v231 offset:56320
	s_nop 0
	global_load_lds_dwordx4 v194, s[0:1]
	s_add_u32 s0, s46, 0x10180
	s_addc_u32 s1, s47, 0
	v_mov_b32_e32 v194, v229
	s_mov_b32 m0, s70
	s_nop 0
	global_load_lds_dwordx4 v194, s[0:1]
	s_barrier
	s_waitcnt lgkmcnt(0)
	s_setprio 1
	s_waitcnt lgkmcnt(0)
	v_mfma_f32_16x16x128_f8f6f4 v[70:73], v[138:145], v[146:153], v[70:73]
	v_mfma_f32_16x16x128_f8f6f4 v[74:77], v[130:137], v[154:161], v[74:77]
	v_mfma_f32_16x16x128_f8f6f4 v[78:81], v[138:145], v[154:161], v[78:81]
	v_mfma_f32_16x16x128_f8f6f4 v[82:85], v[130:137], v[162:169], v[82:85]
	v_mfma_f32_16x16x128_f8f6f4 v[86:89], v[138:145], v[162:169], v[86:89]
	v_mfma_f32_16x16x128_f8f6f4 v[90:93], v[130:137], v[170:177], v[90:93]
	v_mfma_f32_16x16x128_f8f6f4 v[94:97], v[138:145], v[170:177], v[94:97]
	v_mfma_f32_16x16x128_f8f6f4 v[66:69], v[130:137], v[146:153], v[66:69]
	s_setprio 0
	s_barrier
	s_add_u32 s0, s68, 0x8180
	s_addc_u32 s1, s69, 0
	v_mov_b32_e32 v130, v230
	s_mov_b32 m0, s71
	s_nop 0
	global_load_lds_dwordx4 v130, s[0:1]
	s_add_u32 s0, s68, 0x28180
	s_addc_u32 s1, s69, 0
	v_mov_b32_e32 v130, v230
	s_mov_b32 m0, s72
	s_nop 0
	global_load_lds_dwordx4 v130, s[0:1]
	s_waitcnt vmcnt(6)
	s_barrier
	s_setprio 1
	v_mfma_f32_16x16x128_f8f6f4 v[98:101], v[178:185], v[146:153], v[98:101]
	v_mfma_f32_16x16x128_f8f6f4 v[102:105], v[186:193], v[146:153], v[102:105]
	v_mfma_f32_16x16x128_f8f6f4 v[106:109], v[178:185], v[154:161], v[106:109]
	v_mfma_f32_16x16x128_f8f6f4 v[110:113], v[186:193], v[154:161], v[110:113]
	v_mfma_f32_16x16x128_f8f6f4 v[114:117], v[178:185], v[162:169], v[114:117]
	v_mfma_f32_16x16x128_f8f6f4 v[118:121], v[186:193], v[162:169], v[118:121]
	v_mfma_f32_16x16x128_f8f6f4 v[122:125], v[178:185], v[170:177], v[122:125]
	v_mfma_f32_16x16x128_f8f6f4 v[126:129], v[186:193], v[170:177], v[126:129]
	s_setprio 0
	s_barrier
	ds_read_b128 v[130:133], v232
	ds_read_b128 v[134:137], v232 offset:1024
	ds_read_b128 v[138:141], v232 offset:2048
	ds_read_b128 v[142:145], v232 offset:3072
	s_add_u32 s4, s46, 0x200
	s_addc_u32 s5, s47, 0
	s_add_u32 s6, s68, 0x200
	s_addc_u32 s7, s69, 0
	s_add_u32 s0, s46, 0x280
	s_addc_u32 s1, s47, 0
	s_add_u32 s74, s46, 0x20180
	s_addc_u32 s75, s47, 0
	v_mov_b32_e32 v178, v229
	s_mov_b32 m0, s61
	ds_read_b128 v[146:149], v231
	ds_read_b128 v[150:153], v231 offset:1024
	ds_read_b128 v[154:157], v231 offset:2048
	ds_read_b128 v[158:161], v231 offset:3072
	ds_read_b128 v[162:165], v231 offset:4096
	ds_read_b128 v[166:169], v231 offset:5120
	ds_read_b128 v[170:173], v231 offset:6144
	ds_read_b128 v[174:177], v231 offset:7168
	s_nop 0
	global_load_lds_dwordx4 v178, s[74:75]
	s_add_u32 s74, s46, 0x30180
	s_addc_u32 s75, s47, 0
	v_mov_b32_e32 v178, v229
	s_mov_b32 m0, s23
	s_nop 0
	global_load_lds_dwordx4 v178, s[74:75]
	s_waitcnt lgkmcnt(8)
	s_barrier
	s_waitcnt lgkmcnt(0)
	s_setprio 1
	s_waitcnt lgkmcnt(0)
	v_mfma_f32_16x16x128_f8f6f4 v[2:5], v[130:137], v[146:153], v[2:5]
	v_mfma_f32_16x16x128_f8f6f4 v[6:9], v[138:145], v[146:153], v[6:9]
	v_mfma_f32_16x16x128_f8f6f4 v[10:13], v[130:137], v[154:161], v[10:13]
	v_mfma_f32_16x16x128_f8f6f4 v[14:17], v[138:145], v[154:161], v[14:17]
	v_mfma_f32_16x16x128_f8f6f4 v[18:21], v[130:137], v[162:169], v[18:21]
	v_mfma_f32_16x16x128_f8f6f4 v[22:25], v[138:145], v[162:169], v[22:25]
	v_mfma_f32_16x16x128_f8f6f4 v[26:29], v[130:137], v[170:177], v[26:29]
	v_mfma_f32_16x16x128_f8f6f4 v[30:33], v[138:145], v[170:177], v[30:33]
	s_setprio 0
	s_barrier
	v_mov_b32_e32 v194, v230
	s_mov_b32 m0, s16
	ds_read_b128 v[178:181], v232 offset:16384
	ds_read_b128 v[182:185], v232 offset:17408
	ds_read_b128 v[186:189], v232 offset:18432
	ds_read_b128 v[190:193], v232 offset:19456
	s_nop 0
	global_load_lds_dwordx4 v194, s[6:7]
	s_add_u32 s6, s68, 0x20200
	s_addc_u32 s7, s69, 0
	v_mov_b32_e32 v194, v230
	s_mov_b32 m0, s17
	s_nop 0
	global_load_lds_dwordx4 v194, s[6:7]
	s_barrier
	s_waitcnt lgkmcnt(0)
	s_setprio 1
	s_waitcnt lgkmcnt(0)
	v_mfma_f32_16x16x128_f8f6f4 v[34:37], v[178:185], v[146:153], v[34:37]
	v_mfma_f32_16x16x128_f8f6f4 v[38:41], v[186:193], v[146:153], v[38:41]
	v_mfma_f32_16x16x128_f8f6f4 v[42:45], v[178:185], v[154:161], v[42:45]
	v_mfma_f32_16x16x128_f8f6f4 v[46:49], v[186:193], v[154:161], v[46:49]
	v_mfma_f32_16x16x128_f8f6f4 v[50:53], v[178:185], v[162:169], v[50:53]
	v_mfma_f32_16x16x128_f8f6f4 v[54:57], v[186:193], v[162:169], v[54:57]
	v_mfma_f32_16x16x128_f8f6f4 v[58:61], v[178:185], v[170:177], v[58:61]
	v_mfma_f32_16x16x128_f8f6f4 v[62:65], v[186:193], v[170:177], v[62:65]
	s_setprio 0
	v_mov_b32_e32 v194, v229
	s_mov_b32 m0, s15
	s_barrier
	ds_read_b128 v[146:149], v231 offset:16384
	ds_read_b128 v[150:153], v231 offset:17408
	ds_read_b128 v[154:157], v231 offset:18432
	ds_read_b128 v[158:161], v231 offset:19456
	ds_read_b128 v[162:165], v231 offset:20480
	ds_read_b128 v[166:169], v231 offset:21504
	ds_read_b128 v[170:173], v231 offset:22528
	ds_read_b128 v[174:177], v231 offset:23552
	s_nop 0
	global_load_lds_dwordx4 v194, s[4:5]
	s_add_u32 s4, s46, 0x10200
	s_addc_u32 s5, s47, 0
	v_mov_b32_e32 v194, v229
	s_mov_b32 m0, s24
	s_nop 0
	global_load_lds_dwordx4 v194, s[4:5]
	s_barrier
	s_waitcnt lgkmcnt(0)
	s_setprio 1
	s_waitcnt lgkmcnt(0)
	v_mfma_f32_16x16x128_f8f6f4 v[70:73], v[138:145], v[146:153], v[70:73]
	v_mfma_f32_16x16x128_f8f6f4 v[74:77], v[130:137], v[154:161], v[74:77]
	v_mfma_f32_16x16x128_f8f6f4 v[78:81], v[138:145], v[154:161], v[78:81]
	v_mfma_f32_16x16x128_f8f6f4 v[82:85], v[130:137], v[162:169], v[82:85]
	v_mfma_f32_16x16x128_f8f6f4 v[86:89], v[138:145], v[162:169], v[86:89]
	v_mfma_f32_16x16x128_f8f6f4 v[90:93], v[130:137], v[170:177], v[90:93]
	v_mfma_f32_16x16x128_f8f6f4 v[94:97], v[138:145], v[170:177], v[94:97]
	v_mfma_f32_16x16x128_f8f6f4 v[66:69], v[130:137], v[146:153], v[66:69]
	s_setprio 0
	s_barrier
	s_add_u32 s4, s68, 0x8200
	s_addc_u32 s5, s69, 0
	v_mov_b32_e32 v130, v230
	s_mov_b32 m0, s25
	s_nop 0
	global_load_lds_dwordx4 v130, s[4:5]
	s_add_u32 s4, s68, 0x28200
	s_addc_u32 s5, s69, 0
	v_mov_b32_e32 v130, v230
	s_mov_b32 m0, s26
	s_nop 0
	global_load_lds_dwordx4 v130, s[4:5]
	s_waitcnt vmcnt(6)
	s_barrier
	s_setprio 1
	v_mfma_f32_16x16x128_f8f6f4 v[98:101], v[178:185], v[146:153], v[98:101]
	v_mfma_f32_16x16x128_f8f6f4 v[102:105], v[186:193], v[146:153], v[102:105]
	v_mfma_f32_16x16x128_f8f6f4 v[106:109], v[178:185], v[154:161], v[106:109]
	v_mfma_f32_16x16x128_f8f6f4 v[110:113], v[186:193], v[154:161], v[110:113]
	v_mfma_f32_16x16x128_f8f6f4 v[114:117], v[178:185], v[162:169], v[114:117]
	v_mfma_f32_16x16x128_f8f6f4 v[118:121], v[186:193], v[162:169], v[118:121]
	v_mfma_f32_16x16x128_f8f6f4 v[122:125], v[178:185], v[170:177], v[122:125]
	v_mfma_f32_16x16x128_f8f6f4 v[126:129], v[186:193], v[170:177], v[126:129]
	s_setprio 0
	s_barrier
	ds_read_b128 v[130:133], v232 offset:32768
	ds_read_b128 v[134:137], v232 offset:33792
	ds_read_b128 v[138:141], v232 offset:34816
	ds_read_b128 v[142:145], v232 offset:35840
	s_add_u32 s4, s46, 0x20200
	s_addc_u32 s5, s47, 0
	v_mov_b32_e32 v178, v229
	s_mov_b32 m0, s27
	ds_read_b128 v[146:149], v231 offset:32768
	ds_read_b128 v[150:153], v231 offset:33792
	ds_read_b128 v[154:157], v231 offset:34816
	ds_read_b128 v[158:161], v231 offset:35840
	ds_read_b128 v[162:165], v231 offset:36864
	ds_read_b128 v[166:169], v231 offset:37888
	ds_read_b128 v[170:173], v231 offset:38912
	ds_read_b128 v[174:177], v231 offset:39936
	s_nop 0
	global_load_lds_dwordx4 v178, s[4:5]
	s_add_u32 s4, s46, 0x30200
	s_addc_u32 s5, s47, 0
	v_mov_b32_e32 v178, v229
	s_mov_b32 m0, s29
	s_nop 0
	global_load_lds_dwordx4 v178, s[4:5]
	s_waitcnt lgkmcnt(8)
	s_barrier
	s_waitcnt lgkmcnt(0)
	s_setprio 1
	s_waitcnt lgkmcnt(0)
	v_mfma_f32_16x16x128_f8f6f4 v[2:5], v[130:137], v[146:153], v[2:5]
	v_mfma_f32_16x16x128_f8f6f4 v[6:9], v[138:145], v[146:153], v[6:9]
	v_mfma_f32_16x16x128_f8f6f4 v[10:13], v[130:137], v[154:161], v[10:13]
	v_mfma_f32_16x16x128_f8f6f4 v[14:17], v[138:145], v[154:161], v[14:17]
	v_mfma_f32_16x16x128_f8f6f4 v[18:21], v[130:137], v[162:169], v[18:21]
	v_mfma_f32_16x16x128_f8f6f4 v[22:25], v[138:145], v[162:169], v[22:25]
	v_mfma_f32_16x16x128_f8f6f4 v[26:29], v[130:137], v[170:177], v[26:29]
	v_mfma_f32_16x16x128_f8f6f4 v[30:33], v[138:145], v[170:177], v[30:33]
	s_setprio 0
	s_barrier
	s_add_u32 s4, s68, 0x280
	s_addc_u32 s5, s69, 0
	v_mov_b32_e32 v194, v230
	s_mov_b32 m0, s35
	ds_read_b128 v[178:181], v232 offset:49152
	ds_read_b128 v[182:185], v232 offset:50176
	ds_read_b128 v[186:189], v232 offset:51200
	ds_read_b128 v[190:193], v232 offset:52224
	s_nop 0
	global_load_lds_dwordx4 v194, s[4:5]
	s_add_u32 s4, s68, 0x20280
	s_addc_u32 s5, s69, 0
	v_mov_b32_e32 v194, v230
	s_mov_b32 m0, s36
	s_nop 0
	global_load_lds_dwordx4 v194, s[4:5]
	s_barrier
	s_waitcnt lgkmcnt(0)
	s_setprio 1
	s_waitcnt lgkmcnt(0)
	v_mfma_f32_16x16x128_f8f6f4 v[34:37], v[178:185], v[146:153], v[34:37]
	v_mfma_f32_16x16x128_f8f6f4 v[38:41], v[186:193], v[146:153], v[38:41]
	v_mfma_f32_16x16x128_f8f6f4 v[42:45], v[178:185], v[154:161], v[42:45]
	v_mfma_f32_16x16x128_f8f6f4 v[46:49], v[186:193], v[154:161], v[46:49]
	v_mfma_f32_16x16x128_f8f6f4 v[50:53], v[178:185], v[162:169], v[50:53]
	v_mfma_f32_16x16x128_f8f6f4 v[54:57], v[186:193], v[162:169], v[54:57]
	v_mfma_f32_16x16x128_f8f6f4 v[58:61], v[178:185], v[170:177], v[58:61]
	v_mfma_f32_16x16x128_f8f6f4 v[62:65], v[186:193], v[170:177], v[62:65]
	s_setprio 0
	v_mov_b32_e32 v194, v229
	s_mov_b32 m0, s37
	s_barrier
	ds_read_b128 v[146:149], v231 offset:49152
	ds_read_b128 v[150:153], v231 offset:50176
	ds_read_b128 v[154:157], v231 offset:51200
	ds_read_b128 v[158:161], v231 offset:52224
	ds_read_b128 v[162:165], v231 offset:53248
	ds_read_b128 v[166:169], v231 offset:54272
	ds_read_b128 v[170:173], v231 offset:55296
	ds_read_b128 v[174:177], v231 offset:56320
	s_nop 0
	global_load_lds_dwordx4 v194, s[0:1]
	s_add_u32 s0, s46, 0x10280
	s_addc_u32 s1, s47, 0
	v_mov_b32_e32 v194, v229
	s_mov_b32 m0, s70
	s_nop 0
	global_load_lds_dwordx4 v194, s[0:1]
	s_barrier
	s_waitcnt lgkmcnt(0)
	s_setprio 1
	s_waitcnt lgkmcnt(0)
	v_mfma_f32_16x16x128_f8f6f4 v[70:73], v[138:145], v[146:153], v[70:73]
	v_mfma_f32_16x16x128_f8f6f4 v[74:77], v[130:137], v[154:161], v[74:77]
	v_mfma_f32_16x16x128_f8f6f4 v[78:81], v[138:145], v[154:161], v[78:81]
	v_mfma_f32_16x16x128_f8f6f4 v[82:85], v[130:137], v[162:169], v[82:85]
	v_mfma_f32_16x16x128_f8f6f4 v[86:89], v[138:145], v[162:169], v[86:89]
	v_mfma_f32_16x16x128_f8f6f4 v[90:93], v[130:137], v[170:177], v[90:93]
	v_mfma_f32_16x16x128_f8f6f4 v[94:97], v[138:145], v[170:177], v[94:97]
	v_mfma_f32_16x16x128_f8f6f4 v[66:69], v[130:137], v[146:153], v[66:69]
	s_setprio 0
	s_barrier
	s_add_u32 s0, s68, 0x8280
	s_addc_u32 s1, s69, 0
	v_mov_b32_e32 v130, v230
	s_mov_b32 m0, s71
	s_nop 0
	global_load_lds_dwordx4 v130, s[0:1]
	s_add_u32 s0, s68, 0x28280
	s_addc_u32 s1, s69, 0
	v_mov_b32_e32 v130, v230
	s_mov_b32 m0, s72
	s_nop 0
	global_load_lds_dwordx4 v130, s[0:1]
	s_waitcnt vmcnt(6)
	s_barrier
	s_setprio 1
	v_mfma_f32_16x16x128_f8f6f4 v[98:101], v[178:185], v[146:153], v[98:101]
	v_mfma_f32_16x16x128_f8f6f4 v[102:105], v[186:193], v[146:153], v[102:105]
	v_mfma_f32_16x16x128_f8f6f4 v[106:109], v[178:185], v[154:161], v[106:109]
	v_mfma_f32_16x16x128_f8f6f4 v[110:113], v[186:193], v[154:161], v[110:113]
	v_mfma_f32_16x16x128_f8f6f4 v[114:117], v[178:185], v[162:169], v[114:117]
	v_mfma_f32_16x16x128_f8f6f4 v[118:121], v[186:193], v[162:169], v[118:121]
	v_mfma_f32_16x16x128_f8f6f4 v[122:125], v[178:185], v[170:177], v[122:125]
	v_mfma_f32_16x16x128_f8f6f4 v[126:129], v[186:193], v[170:177], v[126:129]
	s_setprio 0
	s_barrier
	ds_read_b128 v[130:133], v232
	ds_read_b128 v[134:137], v232 offset:1024
	ds_read_b128 v[138:141], v232 offset:2048
	ds_read_b128 v[142:145], v232 offset:3072
	s_add_u32 s4, s46, 0x300
	s_addc_u32 s5, s47, 0
	s_add_u32 s6, s68, 0x300
	s_addc_u32 s7, s69, 0
	s_add_u32 s0, s46, 0x380
	s_addc_u32 s1, s47, 0
	s_add_u32 s74, s46, 0x20280
	s_addc_u32 s75, s47, 0
	v_mov_b32_e32 v178, v229
	s_mov_b32 m0, s61
	ds_read_b128 v[146:149], v231
	ds_read_b128 v[150:153], v231 offset:1024
	ds_read_b128 v[154:157], v231 offset:2048
	ds_read_b128 v[158:161], v231 offset:3072
	ds_read_b128 v[162:165], v231 offset:4096
	ds_read_b128 v[166:169], v231 offset:5120
	ds_read_b128 v[170:173], v231 offset:6144
	ds_read_b128 v[174:177], v231 offset:7168
	s_nop 0
	global_load_lds_dwordx4 v178, s[74:75]
	s_add_u32 s74, s46, 0x30280
	s_addc_u32 s75, s47, 0
	v_mov_b32_e32 v178, v229
	s_mov_b32 m0, s23
	s_nop 0
	global_load_lds_dwordx4 v178, s[74:75]
	s_waitcnt lgkmcnt(8)
	s_barrier
	s_waitcnt lgkmcnt(0)
	s_setprio 1
	s_waitcnt lgkmcnt(0)
	v_mfma_f32_16x16x128_f8f6f4 v[2:5], v[130:137], v[146:153], v[2:5]
	v_mfma_f32_16x16x128_f8f6f4 v[6:9], v[138:145], v[146:153], v[6:9]
	v_mfma_f32_16x16x128_f8f6f4 v[10:13], v[130:137], v[154:161], v[10:13]
	v_mfma_f32_16x16x128_f8f6f4 v[14:17], v[138:145], v[154:161], v[14:17]
	v_mfma_f32_16x16x128_f8f6f4 v[18:21], v[130:137], v[162:169], v[18:21]
	v_mfma_f32_16x16x128_f8f6f4 v[22:25], v[138:145], v[162:169], v[22:25]
	v_mfma_f32_16x16x128_f8f6f4 v[26:29], v[130:137], v[170:177], v[26:29]
	v_mfma_f32_16x16x128_f8f6f4 v[30:33], v[138:145], v[170:177], v[30:33]
	s_setprio 0
	s_barrier
	v_mov_b32_e32 v194, v230
	s_mov_b32 m0, s16
	ds_read_b128 v[178:181], v232 offset:16384
	ds_read_b128 v[182:185], v232 offset:17408
	ds_read_b128 v[186:189], v232 offset:18432
	ds_read_b128 v[190:193], v232 offset:19456
	s_nop 0
	global_load_lds_dwordx4 v194, s[6:7]
	s_add_u32 s6, s68, 0x20300
	s_addc_u32 s7, s69, 0
	v_mov_b32_e32 v194, v230
	s_mov_b32 m0, s17
	s_nop 0
	global_load_lds_dwordx4 v194, s[6:7]
	s_barrier
	s_waitcnt lgkmcnt(0)
	s_setprio 1
	s_waitcnt lgkmcnt(0)
	v_mfma_f32_16x16x128_f8f6f4 v[34:37], v[178:185], v[146:153], v[34:37]
	v_mfma_f32_16x16x128_f8f6f4 v[38:41], v[186:193], v[146:153], v[38:41]
	v_mfma_f32_16x16x128_f8f6f4 v[42:45], v[178:185], v[154:161], v[42:45]
	v_mfma_f32_16x16x128_f8f6f4 v[46:49], v[186:193], v[154:161], v[46:49]
	v_mfma_f32_16x16x128_f8f6f4 v[50:53], v[178:185], v[162:169], v[50:53]
	v_mfma_f32_16x16x128_f8f6f4 v[54:57], v[186:193], v[162:169], v[54:57]
	v_mfma_f32_16x16x128_f8f6f4 v[58:61], v[178:185], v[170:177], v[58:61]
	v_mfma_f32_16x16x128_f8f6f4 v[62:65], v[186:193], v[170:177], v[62:65]
	s_setprio 0
	v_mov_b32_e32 v194, v229
	s_mov_b32 m0, s15
	s_barrier
	ds_read_b128 v[146:149], v231 offset:16384
	ds_read_b128 v[150:153], v231 offset:17408
	ds_read_b128 v[154:157], v231 offset:18432
	ds_read_b128 v[158:161], v231 offset:19456
	ds_read_b128 v[162:165], v231 offset:20480
	ds_read_b128 v[166:169], v231 offset:21504
	ds_read_b128 v[170:173], v231 offset:22528
	ds_read_b128 v[174:177], v231 offset:23552
	s_nop 0
	global_load_lds_dwordx4 v194, s[4:5]
	s_add_u32 s4, s46, 0x10300
	s_addc_u32 s5, s47, 0
	v_mov_b32_e32 v194, v229
	s_mov_b32 m0, s24
	s_nop 0
	global_load_lds_dwordx4 v194, s[4:5]
	s_barrier
	s_waitcnt lgkmcnt(0)
	s_setprio 1
	s_waitcnt lgkmcnt(0)
	v_mfma_f32_16x16x128_f8f6f4 v[70:73], v[138:145], v[146:153], v[70:73]
	v_mfma_f32_16x16x128_f8f6f4 v[74:77], v[130:137], v[154:161], v[74:77]
	v_mfma_f32_16x16x128_f8f6f4 v[78:81], v[138:145], v[154:161], v[78:81]
	v_mfma_f32_16x16x128_f8f6f4 v[82:85], v[130:137], v[162:169], v[82:85]
	v_mfma_f32_16x16x128_f8f6f4 v[86:89], v[138:145], v[162:169], v[86:89]
	v_mfma_f32_16x16x128_f8f6f4 v[90:93], v[130:137], v[170:177], v[90:93]
	v_mfma_f32_16x16x128_f8f6f4 v[94:97], v[138:145], v[170:177], v[94:97]
	v_mfma_f32_16x16x128_f8f6f4 v[66:69], v[130:137], v[146:153], v[66:69]
	s_setprio 0
	s_barrier
	s_add_u32 s4, s68, 0x8300
	s_addc_u32 s5, s69, 0
	v_mov_b32_e32 v130, v230
	s_mov_b32 m0, s25
	s_nop 0
	global_load_lds_dwordx4 v130, s[4:5]
	s_add_u32 s4, s68, 0x28300
	s_addc_u32 s5, s69, 0
	v_mov_b32_e32 v130, v230
	s_mov_b32 m0, s26
	s_nop 0
	global_load_lds_dwordx4 v130, s[4:5]
	s_waitcnt vmcnt(6)
	s_barrier
	s_setprio 1
	v_mfma_f32_16x16x128_f8f6f4 v[98:101], v[178:185], v[146:153], v[98:101]
	v_mfma_f32_16x16x128_f8f6f4 v[102:105], v[186:193], v[146:153], v[102:105]
	v_mfma_f32_16x16x128_f8f6f4 v[106:109], v[178:185], v[154:161], v[106:109]
	v_mfma_f32_16x16x128_f8f6f4 v[110:113], v[186:193], v[154:161], v[110:113]
	v_mfma_f32_16x16x128_f8f6f4 v[114:117], v[178:185], v[162:169], v[114:117]
	v_mfma_f32_16x16x128_f8f6f4 v[118:121], v[186:193], v[162:169], v[118:121]
	v_mfma_f32_16x16x128_f8f6f4 v[122:125], v[178:185], v[170:177], v[122:125]
	v_mfma_f32_16x16x128_f8f6f4 v[126:129], v[186:193], v[170:177], v[126:129]
	s_setprio 0
	s_barrier
	ds_read_b128 v[130:133], v232 offset:32768
	ds_read_b128 v[134:137], v232 offset:33792
	ds_read_b128 v[138:141], v232 offset:34816
	ds_read_b128 v[142:145], v232 offset:35840
	s_add_u32 s4, s46, 0x20300
	s_addc_u32 s5, s47, 0
	v_mov_b32_e32 v178, v229
	s_mov_b32 m0, s27
	ds_read_b128 v[146:149], v231 offset:32768
	ds_read_b128 v[150:153], v231 offset:33792
	ds_read_b128 v[154:157], v231 offset:34816
	ds_read_b128 v[158:161], v231 offset:35840
	ds_read_b128 v[162:165], v231 offset:36864
	ds_read_b128 v[166:169], v231 offset:37888
	ds_read_b128 v[170:173], v231 offset:38912
	ds_read_b128 v[174:177], v231 offset:39936
	s_nop 0
	global_load_lds_dwordx4 v178, s[4:5]
	s_add_u32 s4, s46, 0x30300
	s_addc_u32 s5, s47, 0
	v_mov_b32_e32 v178, v229
	s_mov_b32 m0, s29
	s_nop 0
	global_load_lds_dwordx4 v178, s[4:5]
	s_waitcnt lgkmcnt(8)
	s_barrier
	s_waitcnt lgkmcnt(0)
	s_setprio 1
	s_waitcnt lgkmcnt(0)
	v_mfma_f32_16x16x128_f8f6f4 v[2:5], v[130:137], v[146:153], v[2:5]
	v_mfma_f32_16x16x128_f8f6f4 v[6:9], v[138:145], v[146:153], v[6:9]
	v_mfma_f32_16x16x128_f8f6f4 v[10:13], v[130:137], v[154:161], v[10:13]
	v_mfma_f32_16x16x128_f8f6f4 v[14:17], v[138:145], v[154:161], v[14:17]
	v_mfma_f32_16x16x128_f8f6f4 v[18:21], v[130:137], v[162:169], v[18:21]
	v_mfma_f32_16x16x128_f8f6f4 v[22:25], v[138:145], v[162:169], v[22:25]
	v_mfma_f32_16x16x128_f8f6f4 v[26:29], v[130:137], v[170:177], v[26:29]
	v_mfma_f32_16x16x128_f8f6f4 v[30:33], v[138:145], v[170:177], v[30:33]
	s_setprio 0
	s_barrier
	s_add_u32 s4, s68, 0x380
	s_addc_u32 s5, s69, 0
	v_mov_b32_e32 v194, v230
	s_mov_b32 m0, s35
	ds_read_b128 v[178:181], v232 offset:49152
	ds_read_b128 v[182:185], v232 offset:50176
	ds_read_b128 v[186:189], v232 offset:51200
	ds_read_b128 v[190:193], v232 offset:52224
	s_nop 0
	global_load_lds_dwordx4 v194, s[4:5]
	s_add_u32 s4, s68, 0x20380
	s_addc_u32 s5, s69, 0
	v_mov_b32_e32 v194, v230
	s_mov_b32 m0, s36
	s_nop 0
	global_load_lds_dwordx4 v194, s[4:5]
	s_barrier
	s_waitcnt lgkmcnt(0)
	s_setprio 1
	s_waitcnt lgkmcnt(0)
	v_mfma_f32_16x16x128_f8f6f4 v[34:37], v[178:185], v[146:153], v[34:37]
	v_mfma_f32_16x16x128_f8f6f4 v[38:41], v[186:193], v[146:153], v[38:41]
	v_mfma_f32_16x16x128_f8f6f4 v[42:45], v[178:185], v[154:161], v[42:45]
	v_mfma_f32_16x16x128_f8f6f4 v[46:49], v[186:193], v[154:161], v[46:49]
	v_mfma_f32_16x16x128_f8f6f4 v[50:53], v[178:185], v[162:169], v[50:53]
	v_mfma_f32_16x16x128_f8f6f4 v[54:57], v[186:193], v[162:169], v[54:57]
	v_mfma_f32_16x16x128_f8f6f4 v[58:61], v[178:185], v[170:177], v[58:61]
	v_mfma_f32_16x16x128_f8f6f4 v[62:65], v[186:193], v[170:177], v[62:65]
	s_setprio 0
	v_mov_b32_e32 v194, v229
	s_mov_b32 m0, s37
	s_barrier
	ds_read_b128 v[146:149], v231 offset:49152
	ds_read_b128 v[150:153], v231 offset:50176
	ds_read_b128 v[154:157], v231 offset:51200
	ds_read_b128 v[158:161], v231 offset:52224
	ds_read_b128 v[162:165], v231 offset:53248
	ds_read_b128 v[166:169], v231 offset:54272
	ds_read_b128 v[170:173], v231 offset:55296
	ds_read_b128 v[174:177], v231 offset:56320
	s_nop 0
	global_load_lds_dwordx4 v194, s[0:1]
	s_add_u32 s0, s46, 0x10380
	s_addc_u32 s1, s47, 0
	v_mov_b32_e32 v194, v229
	s_mov_b32 m0, s70
	s_nop 0
	global_load_lds_dwordx4 v194, s[0:1]
	s_barrier
	s_waitcnt lgkmcnt(0)
	s_setprio 1
	s_waitcnt lgkmcnt(0)
	v_mfma_f32_16x16x128_f8f6f4 v[70:73], v[138:145], v[146:153], v[70:73]
	v_mfma_f32_16x16x128_f8f6f4 v[74:77], v[130:137], v[154:161], v[74:77]
	v_mfma_f32_16x16x128_f8f6f4 v[78:81], v[138:145], v[154:161], v[78:81]
	v_mfma_f32_16x16x128_f8f6f4 v[82:85], v[130:137], v[162:169], v[82:85]
	v_mfma_f32_16x16x128_f8f6f4 v[86:89], v[138:145], v[162:169], v[86:89]
	v_mfma_f32_16x16x128_f8f6f4 v[90:93], v[130:137], v[170:177], v[90:93]
	v_mfma_f32_16x16x128_f8f6f4 v[94:97], v[138:145], v[170:177], v[94:97]
	v_mfma_f32_16x16x128_f8f6f4 v[66:69], v[130:137], v[146:153], v[66:69]
	s_setprio 0
	s_barrier
	s_add_u32 s0, s68, 0x8380
	s_addc_u32 s1, s69, 0
	v_mov_b32_e32 v130, v230
	s_mov_b32 m0, s71
	s_nop 0
	global_load_lds_dwordx4 v130, s[0:1]
	s_add_u32 s0, s68, 0x28380
	s_addc_u32 s1, s69, 0
	v_mov_b32_e32 v130, v230
	s_mov_b32 m0, s72
	s_nop 0
	global_load_lds_dwordx4 v130, s[0:1]
	s_waitcnt vmcnt(6)
	s_barrier
	s_setprio 1
	v_mfma_f32_16x16x128_f8f6f4 v[98:101], v[178:185], v[146:153], v[98:101]
	v_mfma_f32_16x16x128_f8f6f4 v[102:105], v[186:193], v[146:153], v[102:105]
	v_mfma_f32_16x16x128_f8f6f4 v[106:109], v[178:185], v[154:161], v[106:109]
	v_mfma_f32_16x16x128_f8f6f4 v[110:113], v[186:193], v[154:161], v[110:113]
	v_mfma_f32_16x16x128_f8f6f4 v[114:117], v[178:185], v[162:169], v[114:117]
	v_mfma_f32_16x16x128_f8f6f4 v[118:121], v[186:193], v[162:169], v[118:121]
	v_mfma_f32_16x16x128_f8f6f4 v[122:125], v[178:185], v[170:177], v[122:125]
	v_mfma_f32_16x16x128_f8f6f4 v[126:129], v[186:193], v[170:177], v[126:129]
	s_setprio 0
	s_barrier
	ds_read_b128 v[134:137], v232
	ds_read_b128 v[138:141], v232 offset:1024
	ds_read_b128 v[142:145], v232 offset:2048
	ds_read_b128 v[146:149], v232 offset:3072
	s_add_u32 s0, s44, 0x80
	s_addc_u32 s1, s45, 0
	s_add_u32 s4, s46, 0x20380
	s_addc_u32 s5, s47, 0
	v_mov_b32_e32 v130, v229
	s_mov_b32 m0, s61
	ds_read_b128 v[150:153], v231
	ds_read_b128 v[154:157], v231 offset:1024
	ds_read_b128 v[158:161], v231 offset:2048
	ds_read_b128 v[162:165], v231 offset:3072
	ds_read_b128 v[166:169], v231 offset:4096
	ds_read_b128 v[170:173], v231 offset:5120
	ds_read_b128 v[234:237], v231 offset:6144
	ds_read_b128 v[238:241], v231 offset:7168
	s_nop 0
	global_load_lds_dwordx4 v130, s[4:5]
	s_add_u32 s4, s46, 0x30380
	s_addc_u32 s5, s47, 0
	v_mov_b32_e32 v130, v229
	s_mov_b32 m0, s23
	s_nop 0
	global_load_lds_dwordx4 v130, s[4:5]
	s_waitcnt lgkmcnt(8)
	s_barrier
	s_waitcnt lgkmcnt(0)
	s_setprio 1
	s_waitcnt lgkmcnt(0)
	v_mfma_f32_16x16x128_f8f6f4 v[174:177], v[134:141], v[150:157], v[2:5]
	v_mfma_f32_16x16x128_f8f6f4 v[178:181], v[142:149], v[150:157], v[6:9]
	v_mfma_f32_16x16x128_f8f6f4 v[182:185], v[134:141], v[158:165], v[10:13]
	v_mfma_f32_16x16x128_f8f6f4 v[186:189], v[142:149], v[158:165], v[14:17]
	v_mfma_f32_16x16x128_f8f6f4 v[190:193], v[134:141], v[166:173], v[18:21]
	v_mfma_f32_16x16x128_f8f6f4 v[194:197], v[142:149], v[166:173], v[22:25]
	v_mfma_f32_16x16x128_f8f6f4 v[198:201], v[134:141], v[234:241], v[26:29]
	v_mfma_f32_16x16x128_f8f6f4 v[202:205], v[142:149], v[234:241], v[30:33]
	s_setprio 0
	s_barrier
	s_mov_b64 s[4:5], s[42:43]
	v_mov_b32_e32 v2, v230
	s_mov_b32 m0, s16
	ds_read_b128 v[242:245], v232 offset:16384
	ds_read_b128 v[246:249], v232 offset:17408
	ds_read_b128 v[208:211], v232 offset:18432
	ds_read_b128 v[212:215], v232 offset:19456
	s_nop 0
	global_load_lds_dwordx4 v2, s[4:5]
	s_add_u32 s4, s42, 0x20000
	s_addc_u32 s5, s43, 0
	v_mov_b32_e32 v2, v230
	s_mov_b32 m0, s17
	s_nop 0
	global_load_lds_dwordx4 v2, s[4:5]
	s_barrier
	s_waitcnt lgkmcnt(0)
	s_setprio 1
	s_waitcnt lgkmcnt(0)
	v_mfma_f32_16x16x128_f8f6f4 v[2:5], v[242:249], v[150:157], v[34:37]
	v_mfma_f32_16x16x128_f8f6f4 v[6:9], v[208:215], v[150:157], v[38:41]
	v_mfma_f32_16x16x128_f8f6f4 v[10:13], v[242:249], v[158:165], v[42:45]
	v_mfma_f32_16x16x128_f8f6f4 v[14:17], v[208:215], v[158:165], v[46:49]
	v_mfma_f32_16x16x128_f8f6f4 v[18:21], v[242:249], v[166:173], v[50:53]
	v_mfma_f32_16x16x128_f8f6f4 v[22:25], v[208:215], v[166:173], v[54:57]
	v_mfma_f32_16x16x128_f8f6f4 v[26:29], v[242:249], v[234:241], v[58:61]
	v_mfma_f32_16x16x128_f8f6f4 v[30:33], v[208:215], v[234:241], v[62:65]
	s_setprio 0
	s_mov_b64 s[4:5], s[44:45]
	v_mov_b32_e32 v34, v229
	s_mov_b32 m0, s15
	s_barrier
	s_nop 0
	ds_read_b128 v[58:61], v231 offset:16384
	ds_read_b128 v[62:65], v231 offset:17408
	ds_read_b128 v[154:157], v231 offset:18432
	ds_read_b128 v[158:161], v231 offset:19456
	ds_read_b128 v[162:165], v231 offset:20480
	ds_read_b128 v[166:169], v231 offset:21504
	ds_read_b128 v[234:237], v231 offset:22528
	ds_read_b128 v[238:241], v231 offset:23552
	s_nop 0
	global_load_lds_dwordx4 v34, s[4:5]
	s_add_u32 s4, s44, 0x10000
	s_addc_u32 s5, s45, 0
	v_mov_b32_e32 v34, v229
	s_mov_b32 m0, s24
	s_nop 0
	global_load_lds_dwordx4 v34, s[4:5]
	s_barrier
	s_waitcnt lgkmcnt(0)
	s_setprio 1
	s_waitcnt lgkmcnt(0)
	v_mfma_f32_16x16x128_f8f6f4 v[34:37], v[134:141], v[58:65], v[66:69]
	v_mfma_f32_16x16x128_f8f6f4 v[38:41], v[142:149], v[58:65], v[70:73]
	v_mfma_f32_16x16x128_f8f6f4 v[42:45], v[134:141], v[154:161], v[74:77]
	v_mfma_f32_16x16x128_f8f6f4 v[50:53], v[142:149], v[154:161], v[78:81]
	v_mfma_f32_16x16x128_f8f6f4 v[54:57], v[134:141], v[162:169], v[82:85]
	v_mfma_f32_16x16x128_f8f6f4 v[130:133], v[142:149], v[162:169], v[86:89]
	v_mfma_f32_16x16x128_f8f6f4 v[134:137], v[134:141], v[234:241], v[90:93]
	v_mfma_f32_16x16x128_f8f6f4 v[138:141], v[142:149], v[234:241], v[94:97]
	s_setprio 0
	s_barrier
	s_add_u32 s4, s42, 0x8000
	s_addc_u32 s5, s43, 0
	v_mov_b32_e32 v46, v230
	s_mov_b32 m0, s25
	s_nop 0
	global_load_lds_dwordx4 v46, s[4:5]
	s_add_u32 s4, s42, 0x28000
	s_addc_u32 s5, s43, 0
	v_mov_b32_e32 v46, v230
	s_mov_b32 m0, s26
	s_nop 0
	global_load_lds_dwordx4 v46, s[4:5]
	s_waitcnt vmcnt(6)
	s_barrier
	s_setprio 1
	v_mfma_f32_16x16x128_f8f6f4 v[142:145], v[242:249], v[58:65], v[98:101]
	v_mfma_f32_16x16x128_f8f6f4 v[146:149], v[208:215], v[58:65], v[102:105]
	v_mfma_f32_16x16x128_f8f6f4 v[150:153], v[242:249], v[154:161], v[106:109]
	v_mfma_f32_16x16x128_f8f6f4 v[154:157], v[208:215], v[154:161], v[110:113]
	v_mfma_f32_16x16x128_f8f6f4 v[158:161], v[242:249], v[162:169], v[114:117]
	v_mfma_f32_16x16x128_f8f6f4 v[162:165], v[208:215], v[162:169], v[118:121]
	v_mfma_f32_16x16x128_f8f6f4 v[166:169], v[242:249], v[234:241], v[122:125]
	v_mfma_f32_16x16x128_f8f6f4 v[170:173], v[208:215], v[234:241], v[126:129]
	s_setprio 0
	s_barrier
	ds_read_b128 v[208:211], v232 offset:32768
	ds_read_b128 v[212:215], v232 offset:33792
	ds_read_b128 v[234:237], v232 offset:34816
	ds_read_b128 v[238:241], v232 offset:35840
	s_add_u32 s4, s44, 0x20000
	s_addc_u32 s5, s45, 0
	v_mov_b32_e32 v46, v229
	s_mov_b32 m0, s27
	ds_read_b128 v[58:61], v231 offset:32768
	ds_read_b128 v[62:65], v231 offset:33792
	ds_read_b128 v[242:245], v231 offset:34816
	ds_read_b128 v[246:249], v231 offset:35840
	ds_read_b128 v[216:219], v231 offset:36864
	ds_read_b128 v[220:223], v231 offset:37888
	ds_read_b128 v[66:69], v231 offset:38912
	ds_read_b128 v[70:73], v231 offset:39936
	s_nop 0
	global_load_lds_dwordx4 v46, s[4:5]
	s_add_u32 s4, s44, 0x30000
	s_addc_u32 s5, s45, 0
	v_mov_b32_e32 v46, v229
	s_mov_b32 m0, s29
	s_nop 0
	global_load_lds_dwordx4 v46, s[4:5]
	s_waitcnt lgkmcnt(8)
	s_barrier
	s_waitcnt lgkmcnt(0)
	s_setprio 1
	s_waitcnt lgkmcnt(0)
	v_mfma_f32_16x16x128_f8f6f4 v[126:129], v[208:215], v[58:65], v[174:177]
	v_mfma_f32_16x16x128_f8f6f4 v[122:125], v[234:241], v[58:65], v[178:181]
	v_mfma_f32_16x16x128_f8f6f4 v[106:109], v[208:215], v[242:249], v[182:185]
	v_mfma_f32_16x16x128_f8f6f4 v[98:101], v[234:241], v[242:249], v[186:189]
	v_mfma_f32_16x16x128_f8f6f4 v[90:93], v[208:215], v[216:223], v[190:193]
	v_mfma_f32_16x16x128_f8f6f4 v[82:85], v[234:241], v[216:223], v[194:197]
	v_mfma_f32_16x16x128_f8f6f4 v[74:77], v[208:215], v[66:73], v[198:201]
	v_mfma_f32_16x16x128_f8f6f4 v[174:177], v[234:241], v[66:73], v[202:205]
	s_setprio 0
	s_barrier
	s_add_u32 s4, s42, 0x80
	s_addc_u32 s5, s43, 0
	v_mov_b32_e32 v46, v230
	s_mov_b32 m0, s35
	ds_read_b128 v[178:181], v232 offset:49152
	ds_read_b128 v[182:185], v232 offset:50176
	ds_read_b128 v[186:189], v232 offset:51200
	ds_read_b128 v[190:193], v232 offset:52224
	s_nop 0
	global_load_lds_dwordx4 v46, s[4:5]
	s_add_u32 s4, s42, 0x20080
	s_addc_u32 s5, s43, 0
	v_mov_b32_e32 v46, v230
	s_mov_b32 m0, s36
	s_nop 0
	global_load_lds_dwordx4 v46, s[4:5]
	s_barrier
	s_waitcnt lgkmcnt(0)
	s_setprio 1
	s_waitcnt lgkmcnt(0)
	v_mfma_f32_16x16x128_f8f6f4 v[118:121], v[178:185], v[58:65], v[2:5]
	v_mfma_f32_16x16x128_f8f6f4 v[114:117], v[186:193], v[58:65], v[6:9]
	v_mfma_f32_16x16x128_f8f6f4 v[110:113], v[178:185], v[242:249], v[10:13]
	v_mfma_f32_16x16x128_f8f6f4 v[102:105], v[186:193], v[242:249], v[14:17]
	v_mfma_f32_16x16x128_f8f6f4 v[94:97], v[178:185], v[216:223], v[18:21]
	v_mfma_f32_16x16x128_f8f6f4 v[86:89], v[186:193], v[216:223], v[22:25]
	v_mfma_f32_16x16x128_f8f6f4 v[78:81], v[178:185], v[66:73], v[26:29]
	v_mfma_f32_16x16x128_f8f6f4 v[70:73], v[186:193], v[66:73], v[30:33]
	s_setprio 0
	v_mov_b32_e32 v2, v229
	s_mov_b32 m0, s37
	s_barrier
	ds_read_b128 v[6:9], v231 offset:49152
	ds_read_b128 v[10:13], v231 offset:50176
	ds_read_b128 v[18:21], v231 offset:51200
	ds_read_b128 v[22:25], v231 offset:52224
	ds_read_b128 v[194:197], v231 offset:53248
	ds_read_b128 v[198:201], v231 offset:54272
	ds_read_b128 v[216:219], v231 offset:55296
	ds_read_b128 v[220:223], v231 offset:56320
	s_nop 0
	global_load_lds_dwordx4 v2, s[0:1]
	s_add_u32 s0, s44, 0x10080
	s_addc_u32 s1, s45, 0
	v_mov_b32_e32 v2, v229
	s_mov_b32 m0, s70
	s_nop 0
	global_load_lds_dwordx4 v2, s[0:1]
	s_barrier
	s_waitcnt lgkmcnt(0)
	s_setprio 1
	s_waitcnt lgkmcnt(0)
	v_mfma_f32_16x16x128_f8f6f4 v[62:65], v[208:215], v[6:13], v[34:37]
	v_mfma_f32_16x16x128_f8f6f4 v[58:61], v[234:241], v[6:13], v[38:41]
	v_mfma_f32_16x16x128_f8f6f4 v[46:49], v[208:215], v[18:25], v[42:45]
	v_mfma_f32_16x16x128_f8f6f4 v[42:45], v[234:241], v[18:25], v[50:53]
	v_mfma_f32_16x16x128_f8f6f4 v[30:33], v[208:215], v[194:201], v[54:57]
	v_mfma_f32_16x16x128_f8f6f4 v[26:29], v[234:241], v[194:201], v[130:133]
	v_mfma_f32_16x16x128_f8f6f4 v[2:5], v[208:215], v[216:223], v[134:137]
	v_mfma_f32_16x16x128_f8f6f4 v[14:17], v[234:241], v[216:223], v[138:141]
	s_setprio 0
	s_barrier
	s_add_u32 s0, s42, 0x8080
	s_addc_u32 s1, s43, 0
	v_mov_b32_e32 v34, v230
	s_mov_b32 m0, s71
	s_nop 0
	global_load_lds_dwordx4 v34, s[0:1]
	s_add_u32 s0, s42, 0x28080
	s_addc_u32 s1, s43, 0
	v_mov_b32_e32 v34, v230
	s_mov_b32 m0, s72
	s_nop 0
	global_load_lds_dwordx4 v34, s[0:1]
	s_waitcnt vmcnt(6)
	s_barrier
	s_setprio 1
	v_mfma_f32_16x16x128_f8f6f4 v[54:57], v[178:185], v[6:13], v[142:145]
	v_mfma_f32_16x16x128_f8f6f4 v[50:53], v[186:193], v[6:13], v[146:149]
	v_mfma_f32_16x16x128_f8f6f4 v[38:41], v[178:185], v[18:25], v[150:153]
	v_mfma_f32_16x16x128_f8f6f4 v[34:37], v[186:193], v[18:25], v[154:157]
	v_mfma_f32_16x16x128_f8f6f4 v[22:25], v[178:185], v[194:201], v[158:161]
	v_mfma_f32_16x16x128_f8f6f4 v[18:21], v[186:193], v[194:201], v[162:165]
	v_mfma_f32_16x16x128_f8f6f4 v[10:13], v[178:185], v[216:223], v[166:169]
	v_mfma_f32_16x16x128_f8f6f4 v[6:9], v[186:193], v[216:223], v[170:173]
	s_setprio 0
	s_andn2_b64 vcc, exec, s[54:55]
	s_barrier
	s_cbranch_vccnz .LBB0_123
	s_barrier

.LBB0_574:
	s_lshl_b32 s34, s8, 6
	s_add_u32 s48, s46, 0x3fe00000
	s_addc_u32 s49, s47, 0
	s_add_u32 s8, s4, 0x80
	s_addc_u32 s9, s5, 0
	s_add_i32 s35, s10, 0x18000
	v_mov_b32_e32 v4, v149
	s_waitcnt vmcnt(2)
	s_barrier
	s_mov_b32 m0, s35
	s_mov_b32 s66, 0
	global_load_lds_dwordx4 v4, s[8:9]
	s_add_u32 s8, s4, 0x40080
	s_addc_u32 s9, s5, 0
	v_mov_b32_e32 v4, v149
	s_add_i32 s60, s10, 0x1a000
	s_mov_b32 m0, s60
	v_add_u32_e32 v150, 0, v3
	global_load_lds_dwordx4 v4, s[8:9]
	s_add_u32 s8, s0, 0x80
	s_addc_u32 s9, s1, 0
	v_mov_b32_e32 v4, v148
	s_add_i32 s61, s10, 0x8000
	s_mov_b32 m0, s61
	v_add_u32_e32 v151, 0, v2
	global_load_lds_dwordx4 v4, s[8:9]
	s_add_u32 s8, s0, 0x20080
	s_addc_u32 s9, s1, 0
	v_mov_b32_e32 v4, v148
	s_add_i32 s62, s10, 0xa000
	s_mov_b32 m0, s62
	s_add_i32 s63, s10, 0x1c000
	global_load_lds_dwordx4 v4, s[8:9]
	s_add_u32 s8, s4, 0x10080
	s_addc_u32 s9, s5, 0
	v_mov_b32_e32 v4, v149
	s_mov_b32 m0, s63
	v_readlane_b32 s67, v255, 0
	global_load_lds_dwordx4 v4, s[8:9]
	s_add_u32 s8, s4, 0x50080
	s_addc_u32 s9, s5, 0
	s_add_i32 s64, s10, 0x1e000
	v_mov_b32_e32 v4, v149
	s_mov_b32 m0, s64
	s_cmpk_lt_u32 s6, 0x100
	global_load_lds_dwordx4 v4, s[8:9]
	s_waitcnt vmcnt(0)
	s_cselect_b64 s[50:51], -1, 0
	s_lshl_b32 s65, s7, 6
	v_readlane_b32 s6, v255, 10
	s_mov_b32 s23, s6
	s_barrier
	v_readlane_b32 s7, v255, 11
	s_branch .LBB0_577

.LBB0_579:
	s_ashr_i32 s55, s54, 31
	s_lshl_b64 s[6:7], s[54:55], 19
	s_add_u32 s56, s14, s6
	s_addc_u32 s57, s15, s7
	s_and_b64 s[6:7], s[40:41], exec
	s_cselect_b32 s55, s57, s1
	s_cselect_b32 s68, s56, s0
	s_ashr_i32 s53, s52, 31
	s_lshl_b64 s[6:7], s[52:53], 19
	s_add_u32 s58, s16, s6
	s_addc_u32 s59, s17, s7
	s_and_b64 s[6:7], s[40:41], exec
	s_cselect_b32 s53, s59, s5
	s_cselect_b32 s69, s58, s4
	s_add_u32 s70, s4, 0x100
	v_mov_b32_e32 v2, 0
	s_addc_u32 s71, s5, 0
	s_mov_b32 s72, -2
	v_mov_b32_e32 v3, v2
	v_mov_b32_e32 v4, v2
	v_mov_b32_e32 v5, v2
	v_mov_b32_e32 v6, v2
	v_mov_b32_e32 v7, v2
	v_mov_b32_e32 v8, v2
	v_mov_b32_e32 v9, v2
	v_mov_b32_e32 v18, v2
	v_mov_b32_e32 v19, v2
	v_mov_b32_e32 v20, v2
	v_mov_b32_e32 v21, v2
	v_mov_b32_e32 v22, v2
	v_mov_b32_e32 v23, v2
	v_mov_b32_e32 v24, v2
	v_mov_b32_e32 v25, v2
	v_mov_b32_e32 v42, v2
	v_mov_b32_e32 v43, v2
	v_mov_b32_e32 v44, v2
	v_mov_b32_e32 v45, v2
	v_mov_b32_e32 v46, v2
	v_mov_b32_e32 v47, v2
	v_mov_b32_e32 v48, v2
	v_mov_b32_e32 v49, v2
	v_mov_b32_e32 v66, v2
	v_mov_b32_e32 v67, v2
	v_mov_b32_e32 v68, v2
	s_waitcnt vmcnt(16)
	v_mov_b32_e32 v69, v2
	v_mov_b32_e32 v70, v2
	v_mov_b32_e32 v71, v2
	v_mov_b32_e32 v72, v2
	v_mov_b32_e32 v73, v2
	v_mov_b32_e32 v10, v2
	v_mov_b32_e32 v11, v2
	v_mov_b32_e32 v12, v2
	v_mov_b32_e32 v13, v2
	v_mov_b32_e32 v14, v2
	v_mov_b32_e32 v15, v2
	v_mov_b32_e32 v16, v2
	v_mov_b32_e32 v17, v2
	v_mov_b32_e32 v26, v2
	v_mov_b32_e32 v27, v2
	v_mov_b32_e32 v28, v2
	v_mov_b32_e32 v29, v2
	v_mov_b32_e32 v30, v2
	v_mov_b32_e32 v31, v2
	v_mov_b32_e32 v32, v2
	v_mov_b32_e32 v33, v2
	v_mov_b32_e32 v58, v2
	v_mov_b32_e32 v59, v2
	v_mov_b32_e32 v60, v2
	v_mov_b32_e32 v61, v2
	v_mov_b32_e32 v62, v2
	v_mov_b32_e32 v63, v2
	v_mov_b32_e32 v64, v2
	v_mov_b32_e32 v65, v2
	v_mov_b32_e32 v74, v2
	v_mov_b32_e32 v75, v2
	v_mov_b32_e32 v76, v2
	v_mov_b32_e32 v77, v2
	v_mov_b32_e32 v78, v2
	v_mov_b32_e32 v79, v2
	v_mov_b32_e32 v80, v2
	v_mov_b32_e32 v81, v2
	v_mov_b32_e32 v82, v2
	v_mov_b32_e32 v83, v2
	v_mov_b32_e32 v84, v2
	v_mov_b32_e32 v85, v2
	v_mov_b32_e32 v86, v2
	v_mov_b32_e32 v87, v2
	v_mov_b32_e32 v88, v2
	v_mov_b32_e32 v89, v2
	v_mov_b32_e32 v98, v2
	v_mov_b32_e32 v99, v2
	v_mov_b32_e32 v100, v2
	v_mov_b32_e32 v101, v2
	v_mov_b32_e32 v102, v2
	v_mov_b32_e32 v103, v2
	v_mov_b32_e32 v104, v2
	v_mov_b32_e32 v105, v2
	v_mov_b32_e32 v114, v2
	v_mov_b32_e32 v115, v2
	v_mov_b32_e32 v116, v2
	v_mov_b32_e32 v117, v2
	v_mov_b32_e32 v118, v2
	v_mov_b32_e32 v119, v2
	v_mov_b32_e32 v120, v2
	v_mov_b32_e32 v121, v2
	v_mov_b32_e32 v130, v2
	v_mov_b32_e32 v131, v2
	v_mov_b32_e32 v132, v2
	v_mov_b32_e32 v133, v2
	v_mov_b32_e32 v134, v2
	v_mov_b32_e32 v135, v2
	v_mov_b32_e32 v136, v2
	v_mov_b32_e32 v137, v2
	v_mov_b32_e32 v90, v2
	v_mov_b32_e32 v91, v2
	v_mov_b32_e32 v92, v2
	v_mov_b32_e32 v93, v2
	v_mov_b32_e32 v94, v2
	v_mov_b32_e32 v95, v2
	v_mov_b32_e32 v96, v2
	v_mov_b32_e32 v97, v2
	v_mov_b32_e32 v106, v2
	v_mov_b32_e32 v107, v2
	v_mov_b32_e32 v108, v2
	v_mov_b32_e32 v109, v2
	v_mov_b32_e32 v110, v2
	v_mov_b32_e32 v111, v2
	v_mov_b32_e32 v112, v2
	v_mov_b32_e32 v113, v2
	v_mov_b32_e32 v122, v2
	v_mov_b32_e32 v123, v2
	v_mov_b32_e32 v124, v2
	v_mov_b32_e32 v125, v2
	v_mov_b32_e32 v126, v2
	v_mov_b32_e32 v127, v2
	v_mov_b32_e32 v128, v2
	v_mov_b32_e32 v129, v2
	v_mov_b32_e32 v138, v2
	v_mov_b32_e32 v139, v2
	v_mov_b32_e32 v140, v2
	v_mov_b32_e32 v141, v2
	v_mov_b32_e32 v142, v2
	v_mov_b32_e32 v143, v2
	v_mov_b32_e32 v144, v2
	v_mov_b32_e32 v145, v2

.LBB0_590:
	s_lshl_b32 s35, s10, 6
	s_add_u32 s44, s36, 0x3000
	s_addc_u32 s45, s37, 0
	s_add_u32 s36, s46, 0x57e00000
	s_addc_u32 s37, s47, 0
	s_add_u32 s8, s4, 0x80
	s_addc_u32 s9, s5, 0
	s_add_i32 s58, s24, 0x18000
	v_mov_b32_e32 v4, v138
	s_waitcnt vmcnt(2)
	s_barrier
	s_mov_b32 m0, s58
	s_mov_b32 s66, 0
	global_load_lds_dwordx4 v4, s[8:9]
	s_add_u32 s8, s4, 0x40080
	s_addc_u32 s9, s5, 0
	v_mov_b32_e32 v4, v138
	s_add_i32 s59, s24, 0x1a000
	s_mov_b32 m0, s59
	v_add_u32_e32 v139, 0, v3
	global_load_lds_dwordx4 v4, s[8:9]
	s_add_u32 s8, s0, 0x80
	s_addc_u32 s9, s1, 0
	v_mov_b32_e32 v4, v135
	s_add_i32 s60, s24, 0x8000
	s_mov_b32 m0, s60
	v_add_u32_e32 v140, 0, v2
	global_load_lds_dwordx4 v4, s[8:9]
	s_add_u32 s8, s0, 0x20080
	s_addc_u32 s9, s1, 0
	v_mov_b32_e32 v4, v135
	s_add_i32 s61, s24, 0xa000
	s_mov_b32 m0, s61
	s_add_i32 s62, s24, 0x1c000
	global_load_lds_dwordx4 v4, s[8:9]
	s_add_u32 s8, s4, 0x10080
	s_addc_u32 s9, s5, 0
	v_mov_b32_e32 v4, v138
	s_mov_b32 m0, s62
	v_readlane_b32 s68, v255, 22
	global_load_lds_dwordx4 v4, s[8:9]
	s_add_u32 s8, s4, 0x50080
	s_addc_u32 s9, s5, 0
	s_add_i32 s63, s24, 0x1e000
	v_mov_b32_e32 v4, v138
	s_mov_b32 m0, s63
	s_cmpk_lt_u32 s7, 0x100
	global_load_lds_dwordx4 v4, s[8:9]
	s_cselect_b64 s[48:49], -1, 0
	s_lshl_b32 s64, s6, 6
	s_lshr_b32 s65, s6, 1
	s_lshl_b32 s6, s6, 7
	s_and_b32 s6, s6, 0x80
	s_add_u32 s6, s46, s6
	s_addc_u32 s7, s47, 0
	s_waitcnt vmcnt(0)
	s_add_u32 s46, s6, 0x4be00000
	s_addc_u32 s47, s7, 0
	v_readlane_b32 s6, v255, 25
	s_mov_b32 s67, s6
	s_barrier
	v_readlane_b32 s7, v255, 26
	s_branch .LBB0_593

.LBB0_595:
	s_ashr_i32 s53, s52, 31
	s_lshl_b64 s[6:7], s[52:53], 19
	s_add_u32 s54, s16, s6
	s_addc_u32 s55, s17, s7
	s_and_b64 s[6:7], s[38:39], exec
	s_cselect_b32 s23, s55, s1
	s_cselect_b32 s53, s54, s0
	s_ashr_i32 s51, s50, 31
	s_lshl_b64 s[6:7], s[50:51], 19
	s_add_u32 s56, s14, s6
	s_addc_u32 s57, s15, s7
	s_and_b64 s[6:7], s[38:39], exec
	s_cselect_b32 s51, s57, s5
	s_cselect_b32 s69, s56, s4
	s_add_u32 s70, s4, 0x100
	v_mov_b32_e32 v2, 0
	s_addc_u32 s71, s5, 0
	s_mov_b32 s72, -2
	v_mov_b32_e32 v3, v2
	v_mov_b32_e32 v4, v2
	v_mov_b32_e32 v5, v2
	v_mov_b32_e32 v6, v2
	v_mov_b32_e32 v7, v2
	v_mov_b32_e32 v8, v2
	v_mov_b32_e32 v9, v2
	v_mov_b32_e32 v18, v2
	v_mov_b32_e32 v19, v2
	v_mov_b32_e32 v20, v2
	v_mov_b32_e32 v21, v2
	v_mov_b32_e32 v22, v2
	v_mov_b32_e32 v23, v2
	v_mov_b32_e32 v24, v2
	v_mov_b32_e32 v25, v2
	v_mov_b32_e32 v34, v2
	v_mov_b32_e32 v35, v2
	v_mov_b32_e32 v36, v2
	v_mov_b32_e32 v37, v2
	v_mov_b32_e32 v38, v2
	v_mov_b32_e32 v39, v2
	v_mov_b32_e32 v40, v2
	v_mov_b32_e32 v41, v2
	v_mov_b32_e32 v50, v2
	v_mov_b32_e32 v51, v2
	v_mov_b32_e32 v52, v2
	v_mov_b32_e32 v53, v2
	v_mov_b32_e32 v54, v2
	v_mov_b32_e32 v55, v2
	v_mov_b32_e32 v56, v2
	v_mov_b32_e32 v57, v2
	v_mov_b32_e32 v10, v2
	v_mov_b32_e32 v11, v2
	v_mov_b32_e32 v12, v2
	v_mov_b32_e32 v13, v2
	s_waitcnt vmcnt(2)
	v_mov_b32_e32 v14, v2
	v_mov_b32_e32 v15, v2
	v_mov_b32_e32 v16, v2
	v_mov_b32_e32 v17, v2
	v_mov_b32_e32 v26, v2
	v_mov_b32_e32 v27, v2
	v_mov_b32_e32 v28, v2
	v_mov_b32_e32 v29, v2
	v_mov_b32_e32 v30, v2
	v_mov_b32_e32 v31, v2
	v_mov_b32_e32 v32, v2
	v_mov_b32_e32 v33, v2
	v_mov_b32_e32 v42, v2
	v_mov_b32_e32 v43, v2
	v_mov_b32_e32 v44, v2
	v_mov_b32_e32 v45, v2
	v_mov_b32_e32 v46, v2
	v_mov_b32_e32 v47, v2
	v_mov_b32_e32 v48, v2
	v_mov_b32_e32 v49, v2
	v_mov_b32_e32 v58, v2
	v_mov_b32_e32 v59, v2
	v_mov_b32_e32 v60, v2
	v_mov_b32_e32 v61, v2
	v_mov_b32_e32 v62, v2
	v_mov_b32_e32 v63, v2
	v_mov_b32_e32 v64, v2
	v_mov_b32_e32 v65, v2
	v_mov_b32_e32 v66, v2
	v_mov_b32_e32 v67, v2
	v_mov_b32_e32 v68, v2
	v_mov_b32_e32 v69, v2
	v_mov_b32_e32 v70, v2
	v_mov_b32_e32 v71, v2
	v_mov_b32_e32 v72, v2
	v_mov_b32_e32 v73, v2
	v_mov_b32_e32 v82, v2
	v_mov_b32_e32 v83, v2
	v_mov_b32_e32 v84, v2
	v_mov_b32_e32 v85, v2
	v_mov_b32_e32 v86, v2
	v_mov_b32_e32 v87, v2
	v_mov_b32_e32 v88, v2
	v_mov_b32_e32 v89, v2
	v_mov_b32_e32 v98, v2
	v_mov_b32_e32 v99, v2
	v_mov_b32_e32 v100, v2
	v_mov_b32_e32 v101, v2
	v_mov_b32_e32 v102, v2
	v_mov_b32_e32 v103, v2
	v_mov_b32_e32 v104, v2
	v_mov_b32_e32 v105, v2
	v_mov_b32_e32 v114, v2
	v_mov_b32_e32 v115, v2
	v_mov_b32_e32 v116, v2
	v_mov_b32_e32 v117, v2
	v_mov_b32_e32 v118, v2
	v_mov_b32_e32 v119, v2
	v_mov_b32_e32 v120, v2
	v_mov_b32_e32 v121, v2
	v_mov_b32_e32 v74, v2
	v_mov_b32_e32 v75, v2
	v_mov_b32_e32 v76, v2
	v_mov_b32_e32 v77, v2
	v_mov_b32_e32 v78, v2
	v_mov_b32_e32 v79, v2
	v_mov_b32_e32 v80, v2
	v_mov_b32_e32 v81, v2
	v_mov_b32_e32 v90, v2
	v_mov_b32_e32 v91, v2
	v_mov_b32_e32 v92, v2
	v_mov_b32_e32 v93, v2
	v_mov_b32_e32 v94, v2
	v_mov_b32_e32 v95, v2
	v_mov_b32_e32 v96, v2
	v_mov_b32_e32 v97, v2
	v_mov_b32_e32 v106, v2
	v_mov_b32_e32 v107, v2
	v_mov_b32_e32 v108, v2
	v_mov_b32_e32 v109, v2
	v_mov_b32_e32 v110, v2
	v_mov_b32_e32 v111, v2
	v_mov_b32_e32 v112, v2
	v_mov_b32_e32 v113, v2
	v_mov_b32_e32 v122, v2
	v_mov_b32_e32 v123, v2
	v_mov_b32_e32 v124, v2
	v_mov_b32_e32 v125, v2
	v_mov_b32_e32 v126, v2
	v_mov_b32_e32 v127, v2
	v_mov_b32_e32 v128, v2
	v_mov_b32_e32 v129, v2

.LBB0_1344:
	s_lshl_b32 s34, s10, 6
	s_add_u32 s40, s6, 0x57e00000
	s_addc_u32 s41, s7, 0
	s_add_u32 s42, s6, 0x37d80000
	s_addc_u32 s43, s7, 0
	s_add_u32 s6, s4, 0x80
	s_addc_u32 s7, s5, 0
	s_add_i32 s35, s24, 0x18000
	v_mov_b32_e32 v4, v139
	s_waitcnt vmcnt(2)
	s_barrier
	s_mov_b32 m0, s35
	s_mov_b32 s60, 0
	global_load_lds_dwordx4 v4, s[6:7]
	s_add_u32 s6, s4, 0x40080
	s_addc_u32 s7, s5, 0
	v_mov_b32_e32 v4, v139
	s_add_i32 s36, s24, 0x1a000
	s_mov_b32 m0, s36
	v_add_u32_e32 v140, 0, v3
	global_load_lds_dwordx4 v4, s[6:7]
	s_add_u32 s6, s0, 0x80
	s_addc_u32 s7, s1, 0
	v_mov_b32_e32 v4, v138
	s_add_i32 s37, s24, 0x8000
	s_mov_b32 m0, s37
	v_add_u32_e32 v141, 0, v2
	global_load_lds_dwordx4 v4, s[6:7]
	s_add_u32 s6, s0, 0x20080
	s_addc_u32 s7, s1, 0
	v_mov_b32_e32 v4, v138
	s_add_i32 s56, s24, 0xa000
	s_mov_b32 m0, s56
	s_add_i32 s57, s24, 0x1c000
	global_load_lds_dwordx4 v4, s[6:7]
	s_add_u32 s6, s4, 0x10080
	s_addc_u32 s7, s5, 0
	v_mov_b32_e32 v4, v139
	s_mov_b32 m0, s57
	s_nop 0
	global_load_lds_dwordx4 v4, s[6:7]
	s_add_u32 s6, s4, 0x50080
	s_addc_u32 s7, s5, 0
	s_add_i32 s58, s24, 0x1e000
	v_mov_b32_e32 v4, v139
	s_mov_b32 m0, s58
	s_cmpk_lt_u32 s8, 0x100
	global_load_lds_dwordx4 v4, s[6:7]
	v_readlane_b32 s6, v254, 51
	s_waitcnt vmcnt(0)
	v_readlane_b32 s7, v254, 52
	s_mov_b32 s10, s6
	v_readlane_b32 s6, v254, 47
	s_cselect_b64 s[44:45], -1, 0
	s_lshl_b32 s59, s9, 6
	s_mov_b32 s23, s6
	s_barrier
	v_readlane_b32 s7, v254, 48
	s_branch .LBB0_1347

.LBB0_1349:
	s_ashr_i32 s47, s46, 31
	s_lshl_b64 s[6:7], s[46:47], 19
	s_add_u32 s50, s14, s6
	s_addc_u32 s51, s15, s7
	s_and_b64 s[6:7], s[52:53], exec
	s_cselect_b32 s47, s51, s1
	s_cselect_b32 s61, s50, s0
	s_ashr_i32 s49, s48, 31
	s_lshl_b64 s[6:7], s[48:49], 19
	s_add_u32 s54, s16, s6
	s_addc_u32 s55, s17, s7
	s_and_b64 s[6:7], s[52:53], exec
	s_cselect_b32 s49, s55, s5
	s_cselect_b32 s62, s54, s4
	s_add_u32 s63, s4, 0x100
	v_mov_b32_e32 v10, 0
	s_addc_u32 s64, s5, 0
	s_mov_b32 s65, -2
	v_mov_b32_e32 v11, v10
	v_mov_b32_e32 v12, v10
	v_mov_b32_e32 v13, v10
	s_waitcnt vmcnt(16)
	v_mov_b32_e32 v14, v10
	v_mov_b32_e32 v15, v10
	v_mov_b32_e32 v16, v10
	v_mov_b32_e32 v17, v10
	v_mov_b32_e32 v26, v10
	v_mov_b32_e32 v27, v10
	v_mov_b32_e32 v28, v10
	v_mov_b32_e32 v29, v10
	v_mov_b32_e32 v30, v10
	v_mov_b32_e32 v31, v10
	v_mov_b32_e32 v32, v10
	v_mov_b32_e32 v33, v10
	v_mov_b32_e32 v42, v10
	v_mov_b32_e32 v43, v10
	v_mov_b32_e32 v44, v10
	v_mov_b32_e32 v45, v10
	v_mov_b32_e32 v46, v10
	v_mov_b32_e32 v47, v10
	v_mov_b32_e32 v48, v10
	v_mov_b32_e32 v49, v10
	v_mov_b32_e32 v58, v10
	v_mov_b32_e32 v59, v10
	v_mov_b32_e32 v60, v10
	v_mov_b32_e32 v61, v10
	v_mov_b32_e32 v62, v10
	v_mov_b32_e32 v63, v10
	v_mov_b32_e32 v64, v10
	v_mov_b32_e32 v65, v10
	v_mov_b32_e32 v18, v10
	v_mov_b32_e32 v19, v10
	v_mov_b32_e32 v20, v10
	v_mov_b32_e32 v21, v10
	v_mov_b32_e32 v22, v10
	v_mov_b32_e32 v23, v10
	v_mov_b32_e32 v24, v10
	v_mov_b32_e32 v25, v10
	v_mov_b32_e32 v34, v10
	v_mov_b32_e32 v35, v10
	v_mov_b32_e32 v36, v10
	v_mov_b32_e32 v37, v10
	v_mov_b32_e32 v38, v10
	v_mov_b32_e32 v39, v10
	v_mov_b32_e32 v40, v10
	v_mov_b32_e32 v41, v10
	v_mov_b32_e32 v50, v10
	v_mov_b32_e32 v51, v10
	v_mov_b32_e32 v52, v10
	v_mov_b32_e32 v53, v10
	v_mov_b32_e32 v54, v10
	v_mov_b32_e32 v55, v10
	v_mov_b32_e32 v56, v10
	v_mov_b32_e32 v57, v10
	v_mov_b32_e32 v66, v10
	v_mov_b32_e32 v67, v10
	v_mov_b32_e32 v68, v10
	v_mov_b32_e32 v69, v10
	v_mov_b32_e32 v70, v10
	v_mov_b32_e32 v71, v10
	v_mov_b32_e32 v72, v10
	v_mov_b32_e32 v73, v10
	v_mov_b32_e32 v74, v10
	v_mov_b32_e32 v75, v10
	v_mov_b32_e32 v76, v10
	v_mov_b32_e32 v77, v10
	v_mov_b32_e32 v78, v10
	v_mov_b32_e32 v79, v10
	v_mov_b32_e32 v80, v10
	v_mov_b32_e32 v81, v10
	v_mov_b32_e32 v90, v10
	v_mov_b32_e32 v91, v10
	v_mov_b32_e32 v92, v10
	v_mov_b32_e32 v93, v10
	v_mov_b32_e32 v94, v10
	v_mov_b32_e32 v95, v10
	v_mov_b32_e32 v96, v10
	v_mov_b32_e32 v97, v10
	v_mov_b32_e32 v106, v10
	v_mov_b32_e32 v107, v10
	v_mov_b32_e32 v108, v10
	v_mov_b32_e32 v109, v10
	v_mov_b32_e32 v110, v10
	v_mov_b32_e32 v111, v10
	v_mov_b32_e32 v112, v10
	v_mov_b32_e32 v113, v10
	v_mov_b32_e32 v122, v10
	v_mov_b32_e32 v123, v10
	v_mov_b32_e32 v124, v10
	v_mov_b32_e32 v125, v10
	v_mov_b32_e32 v126, v10
	v_mov_b32_e32 v127, v10
	v_mov_b32_e32 v128, v10
	v_mov_b32_e32 v129, v10
	v_mov_b32_e32 v82, v10
	v_mov_b32_e32 v83, v10
	v_mov_b32_e32 v84, v10
	v_mov_b32_e32 v85, v10
	v_mov_b32_e32 v86, v10
	v_mov_b32_e32 v87, v10
	v_mov_b32_e32 v88, v10
	v_mov_b32_e32 v89, v10
	v_mov_b32_e32 v98, v10
	v_mov_b32_e32 v99, v10
	v_mov_b32_e32 v100, v10
	v_mov_b32_e32 v101, v10
	v_mov_b32_e32 v102, v10
	v_mov_b32_e32 v103, v10
	v_mov_b32_e32 v104, v10
	v_mov_b32_e32 v105, v10
	v_mov_b32_e32 v114, v10
	v_mov_b32_e32 v115, v10
	v_mov_b32_e32 v116, v10
	v_mov_b32_e32 v117, v10
	v_mov_b32_e32 v118, v10
	v_mov_b32_e32 v119, v10
	v_mov_b32_e32 v120, v10
	v_mov_b32_e32 v121, v10
	v_mov_b32_e32 v130, v10
	v_mov_b32_e32 v131, v10
	v_mov_b32_e32 v132, v10
	v_mov_b32_e32 v133, v10
	v_mov_b32_e32 v134, v10
	v_mov_b32_e32 v135, v10
	v_mov_b32_e32 v136, v10
	v_mov_b32_e32 v137, v10
